# speedup vs baseline: 1.0119x; 1.0007x over previous
_Z7kfinal3PKDF16_PKfS2_S2_PK15HIP_vector_typeIjLj4EES2_Pf:
	s_load_dwordx2 s[20:21], s[0:1], 0x20
	v_lshrrev_b32_e32 v48, 6, v0
	s_bfe_u32 s24, s2, 0x20003
	s_mul_i32 s3, s24, 0x28800
	v_lshlrev_b32_e32 v118, 10, v48
	v_and_b32_e32 v1, 63, v0
	s_waitcnt lgkmcnt(0)
	s_add_u32 s6, s20, s3
	v_add_u32_e32 v2, 0, v118
	s_addc_u32 s7, s21, 0
	s_mov_b32 s50, s6
	s_mov_b32 s51, s7
	v_mov_b32_e32 v47, 0
	v_lshlrev_b32_e32 v46, 4, v1
	v_accvgpr_write_b32 a72, v2
	v_add_u32_e32 v8, 0xc600, v2
	v_and_b32_e32 v2, 0x1c0, v0
	v_lshl_add_u64 v[4:5], s[6:7], 0, v[46:47]
	v_lshlrev_b32_e32 v2, 4, v2
	v_mov_b32_e32 v3, v47
	v_readfirstlane_b32 s3, v8
	v_lshl_add_u64 v[6:7], v[4:5], 0, v[2:3]
	s_mov_b32 m0, s3
	v_or_b32_e32 v49, 8, v48
	global_load_lds_dwordx4 v[6:7], off
	s_movk_i32 s3, 0x280
	v_cmp_gt_u32_e64 s[4:5], s3, v0
	v_lshlrev_b32_e32 v90, 10, v49
	s_and_saveexec_b64 s[8:9], s[4:5]
	s_cbranch_execz .LBB3_2
	v_add_u32_e32 v3, 0, v90
	v_add_u32_e32 v3, 0xc600, v3
	v_mov_b32_e32 v91, v47
	v_readfirstlane_b32 s3, v3
	v_lshl_add_u64 v[6:7], v[4:5], 0, v[90:91]
	s_mov_b32 m0, s3
	s_nop 0
	global_load_lds_dwordx4 v[6:7], off

.LBB3_12:
	s_or_b64 exec, exec, s[2:3]
	v_lshlrev_b32_e32 v28, 2, v1
	s_waitcnt lgkmcnt(0)
	global_load_dword v32, v28, s[16:17]
	global_load_dword v31, v28, s[18:19]
	s_movk_i32 s38, 0xff94
	s_movk_i32 s39, 0xffee
	s_add_i32 s40, s22, -4
	v_mov_b32_e32 v131, 0x7f
	v_mov_b32_e32 v132, 0x7c
	v_min_u32_e32 v133, 27, v50
	v_min_u32_e32 v134, 3, v48
	v_or_b32_e32 v134, 24, v134
	v_lshl_or_b32 v128, v48, 6, v1
	v_mul_u32_u24_e32 v129, 0x25f, v128
	v_lshrrev_b32_e32 v129, 16, v129
	v_mad_i32_i24 v128, v129, s38, v128
	v_mul_u32_u24_e32 v130, 0xe39, v128
	v_lshrrev_b32_e32 v130, 16, v130
	v_mad_i32_i24 v128, v130, s39, v128
	v_add_u32_e32 v130, s25, v130
	v_med3_i32 v130, v130, 0, v131
	v_lshl_add_u32 v128, v128, 2, s40
	v_med3_i32 v128, v128, 0, v132
	v_min_u32_e32 v129, 15, v129
	v_lshlrev_b32_e32 v129, 14, v129
	v_lshlrev_b32_e32 v130, 7, v130
	v_or3_b32 v94, v130, v129, v128
	v_lshl_or_b32 v128, v49, 6, v1
	v_mul_u32_u24_e32 v129, 0x25f, v128
	v_lshrrev_b32_e32 v129, 16, v129
	v_mad_i32_i24 v128, v129, s38, v128
	v_mul_u32_u24_e32 v130, 0xe39, v128
	v_lshrrev_b32_e32 v130, 16, v130
	v_mad_i32_i24 v128, v130, s39, v128
	v_add_u32_e32 v130, s25, v130
	v_med3_i32 v130, v130, 0, v131
	v_lshl_add_u32 v128, v128, 2, s40
	v_med3_i32 v128, v128, 0, v132
	v_min_u32_e32 v129, 15, v129
	v_lshlrev_b32_e32 v129, 14, v129
	v_lshlrev_b32_e32 v130, 7, v130
	v_or3_b32 v96, v130, v129, v128
	v_lshl_or_b32 v128, v133, 6, v1
	v_mul_u32_u24_e32 v129, 0x25f, v128
	v_lshrrev_b32_e32 v129, 16, v129
	v_mad_i32_i24 v128, v129, s38, v128
	v_mul_u32_u24_e32 v130, 0xe39, v128
	v_lshrrev_b32_e32 v130, 16, v130
	v_mad_i32_i24 v128, v130, s39, v128
	v_add_u32_e32 v130, s25, v130
	v_med3_i32 v130, v130, 0, v131
	v_lshl_add_u32 v128, v128, 2, s40
	v_med3_i32 v128, v128, 0, v132
	v_min_u32_e32 v129, 15, v129
	v_lshlrev_b32_e32 v129, 14, v129
	v_lshlrev_b32_e32 v130, 7, v130
	v_or3_b32 v98, v130, v129, v128
	v_lshl_or_b32 v128, v134, 6, v1
	v_mul_u32_u24_e32 v129, 0x25f, v128
	v_lshrrev_b32_e32 v129, 16, v129
	v_mad_i32_i24 v128, v129, s38, v128
	v_mul_u32_u24_e32 v130, 0xe39, v128
	v_lshrrev_b32_e32 v130, 16, v130
	v_mad_i32_i24 v128, v130, s39, v128
	v_add_u32_e32 v130, s25, v130
	v_med3_i32 v130, v130, 0, v131
	v_lshl_add_u32 v128, v128, 2, s40
	v_med3_i32 v128, v128, 0, v132
	v_min_u32_e32 v129, 15, v129
	v_lshlrev_b32_e32 v129, 14, v129
	v_lshlrev_b32_e32 v130, 7, v130
	v_or3_b32 v100, v130, v129, v128
	v_cmp_eq_u32_e32 vcc, 27, v134
	v_readfirstlane_b32 s41, v100
	s_nop 1
	v_mov_b32_e32 v135, s41
	v_cndmask_b32_e32 v100, v100, v135, vcc
	v_accvgpr_write_b32 a3, 0
	v_accvgpr_write_b32 a2, 0
	v_accvgpr_write_b32 a1, 0
	v_accvgpr_write_b32 a0, 0
	v_accvgpr_write_b32 a7, 0
	v_accvgpr_write_b32 a6, 0
	v_accvgpr_write_b32 a5, 0
	v_accvgpr_write_b32 a4, 0
	v_accvgpr_write_b32 a15, 0
	v_accvgpr_write_b32 a14, 0
	v_accvgpr_write_b32 a13, 0
	v_accvgpr_write_b32 a12, 0
	v_accvgpr_write_b32 a19, 0
	v_accvgpr_write_b32 a18, 0
	v_accvgpr_write_b32 a17, 0
	v_accvgpr_write_b32 a16, 0
	v_accvgpr_write_b32 a31, 0
	v_accvgpr_write_b32 a30, 0
	v_accvgpr_write_b32 a29, 0
	v_accvgpr_write_b32 a28, 0
	v_accvgpr_write_b32 a63, 0
	v_accvgpr_write_b32 a62, 0
	v_accvgpr_write_b32 a61, 0
	v_accvgpr_write_b32 a60, 0
	v_accvgpr_write_b32 a11, 0
	v_accvgpr_write_b32 a10, 0
	v_accvgpr_write_b32 a9, 0
	v_accvgpr_write_b32 a8, 0
	v_accvgpr_write_b32 a23, 0
	v_accvgpr_write_b32 a22, 0
	v_accvgpr_write_b32 a21, 0
	v_accvgpr_write_b32 a20, 0
	v_accvgpr_write_b32 a27, 0
	v_accvgpr_write_b32 a26, 0
	v_accvgpr_write_b32 a25, 0
	v_accvgpr_write_b32 a24, 0
	v_accvgpr_write_b32 a39, 0
	v_accvgpr_write_b32 a38, 0
	v_accvgpr_write_b32 a37, 0
	v_accvgpr_write_b32 a36, 0
	v_accvgpr_write_b32 a47, 0
	v_accvgpr_write_b32 a46, 0
	v_accvgpr_write_b32 a45, 0
	v_accvgpr_write_b32 a44, 0
	v_accvgpr_write_b32 a67, 0
	v_accvgpr_write_b32 a66, 0
	v_accvgpr_write_b32 a65, 0
	v_accvgpr_write_b32 a64, 0
	v_accvgpr_write_b32 a35, 0
	v_accvgpr_write_b32 a34, 0
	v_accvgpr_write_b32 a33, 0
	v_accvgpr_write_b32 a32, 0
	v_accvgpr_write_b32 a43, 0
	v_accvgpr_write_b32 a42, 0
	v_accvgpr_write_b32 a41, 0
	v_accvgpr_write_b32 a40, 0
	v_accvgpr_write_b32 a51, 0
	v_accvgpr_write_b32 a50, 0
	v_accvgpr_write_b32 a49, 0
	v_accvgpr_write_b32 a48, 0
	v_accvgpr_write_b32 a55, 0
	v_accvgpr_write_b32 a54, 0
	v_accvgpr_write_b32 a53, 0
	v_accvgpr_write_b32 a52, 0
	v_accvgpr_write_b32 a59, 0
	v_accvgpr_write_b32 a58, 0
	v_accvgpr_write_b32 a57, 0
	v_accvgpr_write_b32 a56, 0
	v_accvgpr_write_b32 a71, 0
	v_accvgpr_write_b32 a70, 0
	v_accvgpr_write_b32 a69, 0
	v_accvgpr_write_b32 a68, 0
	v_readfirstlane_b32 s42, v118
	v_and_b32_e32 v130, 63, v0
	v_lshlrev_b32_e32 v130, 4, v130
	v_bfe_u32 v131, v0, 6, 2
	v_bfe_u32 v132, v0, 4, 2
	v_lshrrev_b32_e32 v133, 8, v0
	v_and_b32_e32 v129, 15, v0
	v_lshl_or_b32 v133, v133, 4, v129
	s_add_i32 s43, s42, 0x2000
	s_add_i32 s44, s42, 0x4000
	v_add_u32_e32 v137, s42, v130
	v_add_u32_e32 v138, 0x2000, v137
	v_add_u32_e32 v139, 0x4000, v137
	v_add_u32_e32 v164, 0xc600, v130
	v_add_u32_e32 v165, 0x10e00, v130
	v_add_u32_e32 v166, 0x16000, v130
	v_add_u32_e32 v167, 0x1a800, v130
	v_add_u32_e32 v168, 0x1f000, v130
	s_add_u32 s52, s50, 0x9000
	s_addc_u32 s53, s51, 0
	s_add_i32 m0, s42, 0x16000
	s_nop 0
	global_load_lds_dwordx4 v137, s[52:53]
	s_add_i32 m0, s43, 0x16000
	s_nop 0
	global_load_lds_dwordx4 v138, s[52:53]
	s_cmp_lt_u32 s42, 0x800
	s_cbranch_scc0 .Lk4_sp2
	s_add_i32 m0, s44, 0x16000
	s_nop 0
	global_load_lds_dwordx4 v139, s[52:53]
.Lk4_sp2:
	s_add_u32 s52, s50, 0xd800
	s_addc_u32 s53, s51, 0
	s_add_i32 m0, s42, 0x1a800
	s_nop 0
	global_load_lds_dwordx4 v137, s[52:53]
	s_add_i32 m0, s43, 0x1a800
	s_nop 0
	global_load_lds_dwordx4 v138, s[52:53]
	s_cmp_lt_u32 s42, 0x800
	s_cbranch_scc0 .Lk4_sp3
	s_add_i32 m0, s44, 0x1a800
	s_nop 0
	global_load_lds_dwordx4 v139, s[52:53]
.Lk4_sp3:
	s_add_u32 s52, s50, 0x12000
	s_addc_u32 s53, s51, 0
	s_add_i32 m0, s42, 0x1f000
	s_nop 0
	global_load_lds_dwordx4 v137, s[52:53]
	s_add_i32 m0, s43, 0x1f000
	s_nop 0
	global_load_lds_dwordx4 v138, s[52:53]
	s_cmp_lt_u32 s42, 0x800
	s_cbranch_scc0 .Lk4_sp4
	s_add_i32 m0, s44, 0x1f000
	s_nop 0
	global_load_lds_dwordx4 v139, s[52:53]
.Lk4_sp4:
	v_lshl_add_u32 v128, v131, 1, 0
	v_lshl_add_u32 v128, v128, 5, v128
	v_add3_u32 v128, v128, v133, 0
	v_bitop3_b32 v129, v128, v132, 7 bitop3:0x6c
	v_lshlrev_b32_e32 v128, 7, v128
	v_lshl_or_b32 v140, v129, 4, v128
	v_xor_b32_e32 v141, 64, v140
	v_lshl_add_u32 v128, v131, 1, 1
	v_lshl_add_u32 v128, v128, 5, v128
	v_add3_u32 v128, v128, v133, 0
	v_bitop3_b32 v129, v128, v132, 7 bitop3:0x6c
	v_lshlrev_b32_e32 v128, 7, v128
	v_lshl_or_b32 v142, v129, 4, v128
	v_xor_b32_e32 v143, 64, v142
	v_lshl_add_u32 v128, v131, 1, 0
	v_lshl_add_u32 v128, v128, 5, v128
	v_add3_u32 v128, v128, v133, 1
	v_bitop3_b32 v129, v128, v132, 7 bitop3:0x6c
	v_lshlrev_b32_e32 v128, 7, v128
	v_lshl_or_b32 v144, v129, 4, v128
	v_xor_b32_e32 v145, 64, v144
	v_lshl_add_u32 v128, v131, 1, 1
	v_lshl_add_u32 v128, v128, 5, v128
	v_add3_u32 v128, v128, v133, 1
	v_bitop3_b32 v129, v128, v132, 7 bitop3:0x6c
	v_lshlrev_b32_e32 v128, 7, v128
	v_lshl_or_b32 v146, v129, 4, v128
	v_xor_b32_e32 v147, 64, v146
	v_lshl_add_u32 v128, v131, 1, 2
	v_lshl_add_u32 v128, v128, 5, v128
	v_add3_u32 v128, v128, v133, 0
	v_bitop3_b32 v129, v128, v132, 7 bitop3:0x6c
	v_lshlrev_b32_e32 v128, 7, v128
	v_lshl_or_b32 v148, v129, 4, v128
	v_xor_b32_e32 v149, 64, v148
	v_lshl_add_u32 v128, v131, 1, 3
	v_lshl_add_u32 v128, v128, 5, v128
	v_add3_u32 v128, v128, v133, 0
	v_bitop3_b32 v129, v128, v132, 7 bitop3:0x6c
	v_lshlrev_b32_e32 v128, 7, v128
	v_lshl_or_b32 v150, v129, 4, v128
	v_xor_b32_e32 v151, 64, v150
	v_lshl_add_u32 v128, v131, 1, 2
	v_lshl_add_u32 v128, v128, 5, v128
	v_add3_u32 v128, v128, v133, 1
	v_bitop3_b32 v129, v128, v132, 7 bitop3:0x6c
	v_lshlrev_b32_e32 v128, 7, v128
	v_lshl_or_b32 v152, v129, 4, v128
	v_xor_b32_e32 v153, 64, v152
	v_lshl_add_u32 v128, v131, 1, 3
	v_lshl_add_u32 v128, v128, 5, v128
	v_add3_u32 v128, v128, v133, 1
	v_bitop3_b32 v129, v128, v132, 7 bitop3:0x6c
	v_lshlrev_b32_e32 v128, 7, v128
	v_lshl_or_b32 v154, v129, 4, v128
	v_xor_b32_e32 v155, 64, v154
	v_lshl_add_u32 v128, v131, 1, 4
	v_lshl_add_u32 v128, v128, 5, v128
	v_add3_u32 v128, v128, v133, 0
	v_bitop3_b32 v129, v128, v132, 7 bitop3:0x6c
	v_lshlrev_b32_e32 v128, 7, v128
	v_lshl_or_b32 v156, v129, 4, v128
	v_xor_b32_e32 v157, 64, v156
	v_lshl_add_u32 v128, v131, 1, 5
	v_lshl_add_u32 v128, v128, 5, v128
	v_add3_u32 v128, v128, v133, 0
	v_bitop3_b32 v129, v128, v132, 7 bitop3:0x6c
	v_lshlrev_b32_e32 v128, 7, v128
	v_lshl_or_b32 v158, v129, 4, v128
	v_xor_b32_e32 v159, 64, v158
	v_lshl_add_u32 v128, v131, 1, 4
	v_lshl_add_u32 v128, v128, 5, v128
	v_add3_u32 v128, v128, v133, 1
	v_bitop3_b32 v129, v128, v132, 7 bitop3:0x6c
	v_lshlrev_b32_e32 v128, 7, v128
	v_lshl_or_b32 v160, v129, 4, v128
	v_xor_b32_e32 v161, 64, v160
	v_lshl_add_u32 v128, v131, 1, 5
	v_lshl_add_u32 v128, v128, 5, v128
	v_add3_u32 v128, v128, v133, 1
	v_bitop3_b32 v129, v128, v132, 7 bitop3:0x6c
	v_lshlrev_b32_e32 v128, 7, v128
	v_lshl_or_b32 v162, v129, 4, v128
	v_xor_b32_e32 v163, 64, v162
	s_waitcnt vmcnt(6)
	v_mov_b32_dpp v28, v26 row_shr:1 row_mask:0xf bank_mask:0xf bound_ctrl:1
	v_mov_b32_dpp v29, v27 row_shr:1 row_mask:0xf bank_mask:0xf bound_ctrl:1
	v_pk_add_f32 v[26:27], v[26:27], v[28:29]
	v_mov_b32_e32 v34, 0
	v_mov_b32_e32 v35, 0
	v_mov_b32_dpp v28, v26 row_shr:2 row_mask:0xf bank_mask:0xf bound_ctrl:1
	v_mov_b32_dpp v29, v27 row_shr:2 row_mask:0xf bank_mask:0xf bound_ctrl:1
	v_pk_add_f32 v[26:27], v[26:27], v[28:29]
	v_cmp_eq_u32_e32 vcc, 63, v1
	s_nop 0
	v_mov_b32_dpp v28, v26 row_shr:4 row_mask:0xf bank_mask:0xf bound_ctrl:1
	v_mov_b32_dpp v29, v27 row_shr:4 row_mask:0xf bank_mask:0xf bound_ctrl:1
	v_pk_add_f32 v[26:27], v[26:27], v[28:29]
	s_nop 1
	v_mov_b32_dpp v28, v26 row_shr:8 row_mask:0xf bank_mask:0xf bound_ctrl:1
	v_mov_b32_dpp v29, v27 row_shr:8 row_mask:0xf bank_mask:0xf bound_ctrl:1
	v_pk_add_f32 v[28:29], v[26:27], v[28:29]
	v_mov_b32_e32 v27, 0
	v_mov_b32_e32 v26, 0
	v_mov_b32_dpp v34, v28 row_bcast:15 row_mask:0xa bank_mask:0xf
	v_mov_b32_dpp v35, v29 row_bcast:15 row_mask:0xa bank_mask:0xf
	v_pk_add_f32 v[28:29], v[28:29], v[34:35]
	s_nop 1
	v_mov_b32_dpp v26, v28 row_bcast:31 row_mask:0xc bank_mask:0xf
	v_mov_b32_dpp v27, v29 row_bcast:31 row_mask:0xc bank_mask:0xf
	s_and_saveexec_b64 s[2:3], vcc
	v_lshl_add_u32 v33, v48, 3, 0
	v_add_u32_e32 v33, 0x15800, v33
	v_pk_add_f32 v[26:27], v[28:29], v[26:27]
	ds_write_b64 v33, v[26:27]
	s_or_b64 exec, exec, s[2:3]
	v_cmp_gt_u32_e32 vcc, 64, v0
	s_waitcnt lgkmcnt(0)
	s_barrier
	s_and_saveexec_b64 s[10:11], vcc
	s_cbranch_execz .LBB3_16
	s_add_i32 s2, 0, 0x15800
	v_mov_b32_e32 v26, s2
	s_add_i32 s2, 0, 0x15810
	v_mov_b32_e32 v33, s2
	ds_read_b128 v[26:29], v26
	ds_read_b128 v[34:37], v33
	s_mov_b32 s2, 0xf800000
	s_waitcnt lgkmcnt(1)
	v_add_f32_e32 v26, v26, v28
	s_waitcnt lgkmcnt(0)
	v_add_f32_e32 v28, v34, v36
	v_add_f32_e32 v26, v26, v28
	v_add_f32_e32 v27, v27, v29
	v_add_f32_e32 v28, v35, v37
	v_add_f32_e32 v27, v27, v28
	v_mul_f32_e32 v26, 0x35800000, v26
	v_mul_f32_e32 v27, 0x35800000, v27
	v_fma_f32 v27, -v26, v26, v27
	v_add_f32_e32 v27, 0x3727c5ac, v27
	v_mul_f32_e32 v28, 0x4f800000, v27
	v_cmp_gt_f32_e32 vcc, s2, v27
	s_nop 1
	v_cndmask_b32_e32 v27, v27, v28, vcc
	v_sqrt_f32_e32 v28, v27
	s_nop 0
	v_add_u32_e32 v29, -1, v28
	v_fma_f32 v33, -v29, v28, v27
	v_cmp_ge_f32_e64 s[2:3], 0, v33
	v_add_u32_e32 v33, 1, v28
	s_nop 0
	v_cndmask_b32_e64 v29, v28, v29, s[2:3]
	v_fma_f32 v28, -v33, v28, v27
	v_cmp_lt_f32_e64 s[2:3], 0, v28
	s_nop 1
	v_cndmask_b32_e64 v28, v29, v33, s[2:3]
	v_mul_f32_e32 v29, 0x37800000, v28
	v_cndmask_b32_e32 v28, v28, v29, vcc
	v_mov_b32_e32 v29, 0x260
	v_cmp_class_f32_e32 vcc, v27, v29
	s_nop 1
	v_cndmask_b32_e32 v27, v28, v27, vcc
	v_div_scale_f32 v28, s[2:3], v27, v27, 1.0
	v_rcp_f32_e32 v29, v28
	s_nop 0
	v_fma_f32 v33, -v28, v29, 1.0
	v_fmac_f32_e32 v29, v33, v29
	v_div_scale_f32 v33, vcc, 1.0, v27, 1.0
	v_mul_f32_e32 v34, v33, v29
	v_fma_f32 v35, -v28, v34, v33
	v_fmac_f32_e32 v34, v35, v29
	v_fma_f32 v28, -v28, v34, v33
	v_div_fmas_f32 v28, v28, v29, v34
	v_div_fixup_f32 v27, v28, v27, 1.0
	v_lshl_add_u32 v28, v0, 2, 0
	v_mul_f32_e32 v27, v32, v27
	v_add_u32_e32 v29, 0x15600, v28
	ds_write_b32 v29, v27
	v_fma_f32 v26, -v26, v27, v31
	v_add_u32_e32 v27, 0x15700, v28
	ds_write_b32 v27, v26

.LBB3_20:
	s_or_b64 exec, exec, s[6:7]
	s_load_dwordx2 s[12:13], s[0:1], 0x30
	v_min_u32_e32 v47, 27, v50
	v_min_u32_e32 v2, 3, v48
	v_or_b32_e32 v56, 24, v2
	v_lshrrev_b32_e32 v122, 4, v1
	v_and_b32_e32 v93, 15, v0
	v_lshrrev_b32_e32 v120, 8, v0
	s_lshl_b32 s18, s24, 18
	v_and_b32_e32 v121, 3, v48
	v_lshl_or_b32 v123, v120, 4, v93
	s_movk_i32 s0, 0x42
	s_cmp_lg_u32 0, -1
	v_mad_u32_u24 v1, v121, s0, v123
	s_cselect_b32 s0, 0, 0
	v_lshlrev_b32_e32 v2, 7, v1
	v_bitop3_b32 v3, v1, v122, 7 bitop3:0x6c
	v_add_u32_e32 v1, 33, v1
	s_add_i32 s1, s0, 0xc600
	v_lshl_or_b32 v126, v3, 4, v2
	v_lshlrev_b32_e32 v2, 7, v1
	v_bitop3_b32 v1, v1, v122, 7 bitop3:0x6c
	v_add_u32_e32 v124, s1, v46
	s_add_i32 s1, s0, 0xca00
	v_lshl_or_b32 v127, v1, 4, v2
	v_add_u32_e32 v1, s1, v46
	s_add_i32 s1, s0, 0xce00
	s_waitcnt vmcnt(0)
	s_waitcnt lgkmcnt(0)
	s_barrier
	ds_read_b128 v[42:45], v124
	ds_read_b128 v[38:41], v1
	v_add_u32_e32 v1, s1, v46
	s_add_i32 s1, s0, 0xd200
	ds_read_b128 v[34:37], v1
	v_add_u32_e32 v1, s1, v46
	s_add_i32 s1, s0, 0xd600
	ds_read_b128 v[30:33], v1
	v_add_u32_e32 v1, s1, v46
	s_add_i32 s1, s0, 0xda00
	ds_read_b128 v[26:29], v1
	v_add_u32_e32 v1, s1, v46
	s_add_i32 s1, s0, 0xde00
	ds_read_b128 v[22:25], v1
	v_add_u32_e32 v1, s1, v46
	s_add_i32 s1, s0, 0xe200
	ds_read_b128 v[10:13], v1
	v_add_u32_e32 v1, s1, v46
	s_add_i32 s1, s0, 0xe600
	ds_read_b128 v[6:9], v1
	v_add_u32_e32 v1, s1, v46
	ds_read_b128 v[2:5], v1
	v_add_u32_e32 v1, s0, v126
	ds_read_b128 v[14:17], v1
	v_add_u32_e32 v1, s0, v127
	s_add_i32 s0, s0, 0xea00
	v_add_u32_e32 v125, s0, v46
	s_lshl_b32 s0, s24, 20
	s_add_u32 s10, s2, s0
	v_mov_b32_e32 v95, 0
	v_lshlrev_b32_e32 v0, 4, v0
	ds_read_b128 v[18:21], v1
	s_addc_u32 s11, s3, 0
	v_lshlrev_b32_e32 v91, 10, v47
	v_and_b32_e32 v0, 0x1c00, v0
	v_mov_b32_e32 v1, v95
	v_mov_b32_e32 v47, 0x28800
	s_add_u32 s0, s10, 0x400000
	v_mad_u64_u32 v[54:55], s[2:3], s24, v47, v[0:1]
	s_addc_u32 s1, s11, 0
	v_lshlrev_b32_e32 v48, 2, v94
	v_mov_b32_e32 v49, v95
	v_lshlrev_b32_e32 v50, 2, v96
	v_mov_b32_e32 v51, v95
	v_lshlrev_b32_e32 v52, 2, v98
	v_mov_b32_e32 v53, v95
	v_or_b32_e32 v54, v54, v46
	v_lshlrev_b32_e32 v46, 2, v100
	v_mov_b32_e32 v47, v95
	s_waitcnt lgkmcnt(0)
	v_lshl_add_u64 v[0:1], s[0:1], 0, v[48:49]
	v_lshl_add_u64 v[106:107], s[0:1], 0, v[50:51]
	v_lshl_add_u64 v[110:111], s[0:1], 0, v[52:53]
	v_lshl_add_u64 v[112:113], s[10:11], 0, v[46:47]
	v_lshl_add_u64 v[114:115], s[0:1], 0, v[46:47]
	v_lshl_add_u64 v[46:47], s[20:21], 0, v[54:55]
	s_mov_b64 s[0:1], 0xd000
	v_lshl_add_u64 v[116:117], v[46:47], 0, s[0:1]
	s_movk_i32 s0, 0xc000
	s_movk_i32 s2, 0xe000
	s_mov_b32 s19, 0
	v_lshl_add_u64 v[102:103], s[10:11], 0, v[48:49]
	v_mov_b32_e32 v97, v95
	v_mov_b32_e32 v99, v95
	v_mov_b32_e32 v101, v95
	v_lshlrev_b32_e32 v119, 10, v56
	v_lshl_add_u64 v[104:105], s[10:11], 0, v[50:51]
	v_lshl_add_u64 v[108:109], s[10:11], 0, v[52:53]
	s_mov_b32 s20, 1
	s_mov_b32 s1, -1
	s_mov_b32 s3, -1
	s_add_i32 s17, 0, 0x16000
	s_add_i32 s16, 0, 0x1d000
	s_mov_b64 s[6:7], 0x4800
	s_cmp_ge_u32 s42, 0x1000
	s_cbranch_scc0 .Lk4_noprio
	s_setprio 1
.Lk4_noprio:
	v_mfma_f32_16x16x32_f16 a[0:3], v[42:45], v[14:17], a[0:3]
	ds_read_b128 v[82:85], v141
	v_mfma_f32_16x16x32_f16 a[4:7], v[42:45], v[18:21], a[4:7]
	ds_read_b128 v[86:89], v143
	v_mfma_f32_16x16x32_f16 a[12:15], v[38:41], v[14:17], a[12:15]
	ds_read_b128 v[70:73], v164 offset:9216
	v_mfma_f32_16x16x32_f16 a[16:19], v[38:41], v[18:21], a[16:19]
	ds_read_b128 v[66:69], v164 offset:10240
	v_mfma_f32_16x16x32_f16 a[28:31], v[34:37], v[14:17], a[28:31]
	ds_read_b128 v[58:61], v164 offset:11264
	v_mfma_f32_16x16x32_f16 a[60:63], v[34:37], v[18:21], a[60:63]
	ds_read_b128 v[54:57], v164 offset:12288
	v_mfma_f32_16x16x32_f16 a[8:11], v[30:33], v[14:17], a[8:11]
	ds_read_b128 v[46:49], v164 offset:13312
	v_mfma_f32_16x16x32_f16 a[20:23], v[30:33], v[18:21], a[20:23]
	ds_read_b128 v[50:53], v164 offset:14336
	v_mfma_f32_16x16x32_f16 a[24:27], v[26:29], v[14:17], a[24:27]
	ds_read_b128 v[62:65], v164 offset:15360
	v_mfma_f32_16x16x32_f16 a[36:39], v[26:29], v[18:21], a[36:39]
	ds_read_b128 v[74:77], v164 offset:16384
	v_mfma_f32_16x16x32_f16 a[44:47], v[22:25], v[14:17], a[44:47]
	ds_read_b128 v[78:81], v164 offset:17408
	v_mfma_f32_16x16x32_f16 a[64:67], v[22:25], v[18:21], a[64:67]
	v_mfma_f32_16x16x32_f16 a[32:35], v[10:13], v[14:17], a[32:35]
	v_mfma_f32_16x16x32_f16 a[40:43], v[10:13], v[18:21], a[40:43]
	v_mfma_f32_16x16x32_f16 a[48:51], v[6:9], v[14:17], a[48:51]
	v_mfma_f32_16x16x32_f16 a[52:55], v[6:9], v[18:21], a[52:55]
	v_mfma_f32_16x16x32_f16 a[56:59], v[2:5], v[14:17], a[56:59]
	v_mfma_f32_16x16x32_f16 a[68:71], v[2:5], v[18:21], a[68:71]
	s_waitcnt lgkmcnt(8)
	v_mfma_f32_16x16x32_f16 a[0:3], v[70:73], v[82:85], a[0:3]
	ds_read_b128 v[14:17], v142
	v_mfma_f32_16x16x32_f16 a[4:7], v[70:73], v[86:89], a[4:7]
	ds_read_b128 v[18:21], v144
	s_waitcnt lgkmcnt(9)
	v_mfma_f32_16x16x32_f16 a[12:15], v[66:69], v[82:85], a[12:15]
	ds_read_b128 v[42:45], v165
	v_mfma_f32_16x16x32_f16 a[16:19], v[66:69], v[86:89], a[16:19]
	ds_read_b128 v[38:41], v165 offset:1024
	s_waitcnt lgkmcnt(10)
	v_mfma_f32_16x16x32_f16 a[28:31], v[58:61], v[82:85], a[28:31]
	ds_read_b128 v[34:37], v165 offset:2048
	v_mfma_f32_16x16x32_f16 a[60:63], v[58:61], v[86:89], a[60:63]
	ds_read_b128 v[30:33], v165 offset:3072
	s_waitcnt lgkmcnt(11)
	v_mfma_f32_16x16x32_f16 a[8:11], v[54:57], v[82:85], a[8:11]
	ds_read_b128 v[26:29], v165 offset:4096
	v_mfma_f32_16x16x32_f16 a[20:23], v[54:57], v[86:89], a[20:23]
	ds_read_b128 v[22:25], v165 offset:5120
	s_waitcnt lgkmcnt(12)
	v_mfma_f32_16x16x32_f16 a[24:27], v[46:49], v[82:85], a[24:27]
	ds_read_b128 v[10:13], v165 offset:6144
	v_mfma_f32_16x16x32_f16 a[36:39], v[46:49], v[86:89], a[36:39]
	ds_read_b128 v[6:9], v165 offset:7168
	s_waitcnt lgkmcnt(13)
	v_mfma_f32_16x16x32_f16 a[44:47], v[50:53], v[82:85], a[44:47]
	ds_read_b128 v[2:5], v165 offset:8192
	v_mfma_f32_16x16x32_f16 a[64:67], v[50:53], v[86:89], a[64:67]
	s_waitcnt lgkmcnt(13)
	v_mfma_f32_16x16x32_f16 a[32:35], v[62:65], v[82:85], a[32:35]
	v_mfma_f32_16x16x32_f16 a[40:43], v[62:65], v[86:89], a[40:43]
	s_waitcnt lgkmcnt(12)
	v_mfma_f32_16x16x32_f16 a[48:51], v[74:77], v[82:85], a[48:51]
	v_mfma_f32_16x16x32_f16 a[52:55], v[74:77], v[86:89], a[52:55]
	s_waitcnt lgkmcnt(11)
	v_mfma_f32_16x16x32_f16 a[56:59], v[78:81], v[82:85], a[56:59]
	v_mfma_f32_16x16x32_f16 a[68:71], v[78:81], v[86:89], a[68:71]
	s_waitcnt lgkmcnt(8)
	v_mfma_f32_16x16x32_f16 a[0:3], v[42:45], v[14:17], a[0:3]
	ds_read_b128 v[82:85], v143
	v_mfma_f32_16x16x32_f16 a[4:7], v[42:45], v[18:21], a[4:7]
	ds_read_b128 v[86:89], v145
	s_waitcnt lgkmcnt(9)
	v_mfma_f32_16x16x32_f16 a[12:15], v[38:41], v[14:17], a[12:15]
	ds_read_b128 v[70:73], v165 offset:9216
	v_mfma_f32_16x16x32_f16 a[16:19], v[38:41], v[18:21], a[16:19]
	ds_read_b128 v[66:69], v165 offset:10240
	s_waitcnt lgkmcnt(10)
	v_mfma_f32_16x16x32_f16 a[28:31], v[34:37], v[14:17], a[28:31]
	ds_read_b128 v[58:61], v165 offset:11264
	v_mfma_f32_16x16x32_f16 a[60:63], v[34:37], v[18:21], a[60:63]
	ds_read_b128 v[54:57], v165 offset:12288
	s_waitcnt lgkmcnt(11)
	v_mfma_f32_16x16x32_f16 a[8:11], v[30:33], v[14:17], a[8:11]
	ds_read_b128 v[46:49], v165 offset:13312
	v_mfma_f32_16x16x32_f16 a[20:23], v[30:33], v[18:21], a[20:23]
	ds_read_b128 v[50:53], v165 offset:14336
	s_waitcnt lgkmcnt(12)
	v_mfma_f32_16x16x32_f16 a[24:27], v[26:29], v[14:17], a[24:27]
	ds_read_b128 v[62:65], v165 offset:15360
	v_mfma_f32_16x16x32_f16 a[36:39], v[26:29], v[18:21], a[36:39]
	ds_read_b128 v[74:77], v165 offset:16384
	s_waitcnt lgkmcnt(13)
	v_mfma_f32_16x16x32_f16 a[44:47], v[22:25], v[14:17], a[44:47]
	ds_read_b128 v[78:81], v165 offset:17408
	v_mfma_f32_16x16x32_f16 a[64:67], v[22:25], v[18:21], a[64:67]
	s_waitcnt lgkmcnt(13)
	v_mfma_f32_16x16x32_f16 a[32:35], v[10:13], v[14:17], a[32:35]
	v_mfma_f32_16x16x32_f16 a[40:43], v[10:13], v[18:21], a[40:43]
	s_waitcnt lgkmcnt(12)
	v_mfma_f32_16x16x32_f16 a[48:51], v[6:9], v[14:17], a[48:51]
	v_mfma_f32_16x16x32_f16 a[52:55], v[6:9], v[18:21], a[52:55]
	s_waitcnt lgkmcnt(11)
	v_mfma_f32_16x16x32_f16 a[56:59], v[2:5], v[14:17], a[56:59]
	v_mfma_f32_16x16x32_f16 a[68:71], v[2:5], v[18:21], a[68:71]
	s_waitcnt vmcnt(0) lgkmcnt(0)
	s_barrier
	s_add_u32 s52, s50, 0x16800
	s_addc_u32 s53, s51, 0
	s_add_i32 m0, s42, 0xc600
	s_nop 0
	global_load_lds_dwordx4 v137, s[52:53]
	s_add_i32 m0, s43, 0xc600
	s_nop 0
	global_load_lds_dwordx4 v138, s[52:53]
	s_cmp_lt_u32 s42, 0x800
	s_cbranch_scc0 .Lk4_st1_5
	s_add_i32 m0, s44, 0xc600
	s_nop 0
	global_load_lds_dwordx4 v139, s[52:53]
.Lk4_st1_5:
	s_add_u32 s52, s50, 0x1b000
	s_addc_u32 s53, s51, 0
	s_add_i32 m0, s42, 0x10e00
	s_nop 0
	global_load_lds_dwordx4 v137, s[52:53]
	s_add_i32 m0, s43, 0x10e00
	s_nop 0
	global_load_lds_dwordx4 v138, s[52:53]
	s_cmp_lt_u32 s42, 0x800
	s_cbranch_scc0 .Lk4_st1_6
	s_add_i32 m0, s44, 0x10e00
	s_nop 0
	global_load_lds_dwordx4 v139, s[52:53]
.Lk4_st1_6:
	v_mfma_f32_16x16x32_f16 a[0:3], v[70:73], v[82:85], a[0:3]
	ds_read_b128 v[14:17], v144
	v_mfma_f32_16x16x32_f16 a[4:7], v[70:73], v[86:89], a[4:7]
	ds_read_b128 v[18:21], v146
	v_mfma_f32_16x16x32_f16 a[12:15], v[66:69], v[82:85], a[12:15]
	ds_read_b128 v[42:45], v166
	v_mfma_f32_16x16x32_f16 a[16:19], v[66:69], v[86:89], a[16:19]
	ds_read_b128 v[38:41], v166 offset:1024
	v_mfma_f32_16x16x32_f16 a[28:31], v[58:61], v[82:85], a[28:31]
	ds_read_b128 v[34:37], v166 offset:2048
	v_mfma_f32_16x16x32_f16 a[60:63], v[58:61], v[86:89], a[60:63]
	ds_read_b128 v[30:33], v166 offset:3072
	v_mfma_f32_16x16x32_f16 a[8:11], v[54:57], v[82:85], a[8:11]
	ds_read_b128 v[26:29], v166 offset:4096
	v_mfma_f32_16x16x32_f16 a[20:23], v[54:57], v[86:89], a[20:23]
	ds_read_b128 v[22:25], v166 offset:5120
	v_mfma_f32_16x16x32_f16 a[24:27], v[46:49], v[82:85], a[24:27]
	ds_read_b128 v[10:13], v166 offset:6144
	v_mfma_f32_16x16x32_f16 a[36:39], v[46:49], v[86:89], a[36:39]
	ds_read_b128 v[6:9], v166 offset:7168
	v_mfma_f32_16x16x32_f16 a[44:47], v[50:53], v[82:85], a[44:47]
	ds_read_b128 v[2:5], v166 offset:8192
	v_mfma_f32_16x16x32_f16 a[64:67], v[50:53], v[86:89], a[64:67]
	v_mfma_f32_16x16x32_f16 a[32:35], v[62:65], v[82:85], a[32:35]
	v_mfma_f32_16x16x32_f16 a[40:43], v[62:65], v[86:89], a[40:43]
	v_mfma_f32_16x16x32_f16 a[48:51], v[74:77], v[82:85], a[48:51]
	v_mfma_f32_16x16x32_f16 a[52:55], v[74:77], v[86:89], a[52:55]
	v_mfma_f32_16x16x32_f16 a[56:59], v[78:81], v[82:85], a[56:59]
	v_mfma_f32_16x16x32_f16 a[68:71], v[78:81], v[86:89], a[68:71]
	s_waitcnt lgkmcnt(8)
	v_mfma_f32_16x16x32_f16 a[0:3], v[42:45], v[14:17], a[0:3]
	ds_read_b128 v[82:85], v145
	v_mfma_f32_16x16x32_f16 a[4:7], v[42:45], v[18:21], a[4:7]
	ds_read_b128 v[86:89], v147
	s_waitcnt lgkmcnt(9)
	v_mfma_f32_16x16x32_f16 a[12:15], v[38:41], v[14:17], a[12:15]
	ds_read_b128 v[70:73], v166 offset:9216
	v_mfma_f32_16x16x32_f16 a[16:19], v[38:41], v[18:21], a[16:19]
	ds_read_b128 v[66:69], v166 offset:10240
	s_waitcnt lgkmcnt(10)
	v_mfma_f32_16x16x32_f16 a[28:31], v[34:37], v[14:17], a[28:31]
	ds_read_b128 v[58:61], v166 offset:11264
	v_mfma_f32_16x16x32_f16 a[60:63], v[34:37], v[18:21], a[60:63]
	ds_read_b128 v[54:57], v166 offset:12288
	s_waitcnt lgkmcnt(11)
	v_mfma_f32_16x16x32_f16 a[8:11], v[30:33], v[14:17], a[8:11]
	ds_read_b128 v[46:49], v166 offset:13312
	v_mfma_f32_16x16x32_f16 a[20:23], v[30:33], v[18:21], a[20:23]
	ds_read_b128 v[50:53], v166 offset:14336
	s_waitcnt lgkmcnt(12)
	v_mfma_f32_16x16x32_f16 a[24:27], v[26:29], v[14:17], a[24:27]
	ds_read_b128 v[62:65], v166 offset:15360
	v_mfma_f32_16x16x32_f16 a[36:39], v[26:29], v[18:21], a[36:39]
	ds_read_b128 v[74:77], v166 offset:16384
	s_waitcnt lgkmcnt(13)
	v_mfma_f32_16x16x32_f16 a[44:47], v[22:25], v[14:17], a[44:47]
	ds_read_b128 v[78:81], v166 offset:17408
	v_mfma_f32_16x16x32_f16 a[64:67], v[22:25], v[18:21], a[64:67]
	s_waitcnt lgkmcnt(13)
	v_mfma_f32_16x16x32_f16 a[32:35], v[10:13], v[14:17], a[32:35]
	v_mfma_f32_16x16x32_f16 a[40:43], v[10:13], v[18:21], a[40:43]
	s_waitcnt lgkmcnt(12)
	v_mfma_f32_16x16x32_f16 a[48:51], v[6:9], v[14:17], a[48:51]
	v_mfma_f32_16x16x32_f16 a[52:55], v[6:9], v[18:21], a[52:55]
	s_waitcnt lgkmcnt(11)
	v_mfma_f32_16x16x32_f16 a[56:59], v[2:5], v[14:17], a[56:59]
	v_mfma_f32_16x16x32_f16 a[68:71], v[2:5], v[18:21], a[68:71]
	s_waitcnt lgkmcnt(8)
	v_mfma_f32_16x16x32_f16 a[0:3], v[70:73], v[82:85], a[0:3]
	ds_read_b128 v[14:17], v148
	v_mfma_f32_16x16x32_f16 a[4:7], v[70:73], v[86:89], a[4:7]
	ds_read_b128 v[18:21], v150
	s_waitcnt lgkmcnt(9)
	v_mfma_f32_16x16x32_f16 a[12:15], v[66:69], v[82:85], a[12:15]
	ds_read_b128 v[42:45], v167
	v_mfma_f32_16x16x32_f16 a[16:19], v[66:69], v[86:89], a[16:19]
	ds_read_b128 v[38:41], v167 offset:1024
	s_waitcnt lgkmcnt(10)
	v_mfma_f32_16x16x32_f16 a[28:31], v[58:61], v[82:85], a[28:31]
	ds_read_b128 v[34:37], v167 offset:2048
	v_mfma_f32_16x16x32_f16 a[60:63], v[58:61], v[86:89], a[60:63]
	ds_read_b128 v[30:33], v167 offset:3072
	s_waitcnt lgkmcnt(11)
	v_mfma_f32_16x16x32_f16 a[8:11], v[54:57], v[82:85], a[8:11]
	ds_read_b128 v[26:29], v167 offset:4096
	v_mfma_f32_16x16x32_f16 a[20:23], v[54:57], v[86:89], a[20:23]
	ds_read_b128 v[22:25], v167 offset:5120
	s_waitcnt lgkmcnt(12)
	v_mfma_f32_16x16x32_f16 a[24:27], v[46:49], v[82:85], a[24:27]
	ds_read_b128 v[10:13], v167 offset:6144
	v_mfma_f32_16x16x32_f16 a[36:39], v[46:49], v[86:89], a[36:39]
	ds_read_b128 v[6:9], v167 offset:7168
	s_waitcnt lgkmcnt(13)
	v_mfma_f32_16x16x32_f16 a[44:47], v[50:53], v[82:85], a[44:47]
	ds_read_b128 v[2:5], v167 offset:8192
	v_mfma_f32_16x16x32_f16 a[64:67], v[50:53], v[86:89], a[64:67]
	s_waitcnt lgkmcnt(13)
	v_mfma_f32_16x16x32_f16 a[32:35], v[62:65], v[82:85], a[32:35]
	v_mfma_f32_16x16x32_f16 a[40:43], v[62:65], v[86:89], a[40:43]
	s_waitcnt lgkmcnt(12)
	v_mfma_f32_16x16x32_f16 a[48:51], v[74:77], v[82:85], a[48:51]
	v_mfma_f32_16x16x32_f16 a[52:55], v[74:77], v[86:89], a[52:55]
	s_waitcnt lgkmcnt(11)
	v_mfma_f32_16x16x32_f16 a[56:59], v[78:81], v[82:85], a[56:59]
	v_mfma_f32_16x16x32_f16 a[68:71], v[78:81], v[86:89], a[68:71]
	s_waitcnt lgkmcnt(8)
	v_mfma_f32_16x16x32_f16 a[0:3], v[42:45], v[14:17], a[0:3]
	ds_read_b128 v[82:85], v149
	v_mfma_f32_16x16x32_f16 a[4:7], v[42:45], v[18:21], a[4:7]
	ds_read_b128 v[86:89], v151
	s_waitcnt lgkmcnt(9)
	v_mfma_f32_16x16x32_f16 a[12:15], v[38:41], v[14:17], a[12:15]
	ds_read_b128 v[70:73], v167 offset:9216
	v_mfma_f32_16x16x32_f16 a[16:19], v[38:41], v[18:21], a[16:19]
	ds_read_b128 v[66:69], v167 offset:10240
	s_waitcnt lgkmcnt(10)
	v_mfma_f32_16x16x32_f16 a[28:31], v[34:37], v[14:17], a[28:31]
	ds_read_b128 v[58:61], v167 offset:11264
	v_mfma_f32_16x16x32_f16 a[60:63], v[34:37], v[18:21], a[60:63]
	ds_read_b128 v[54:57], v167 offset:12288
	s_waitcnt lgkmcnt(11)
	v_mfma_f32_16x16x32_f16 a[8:11], v[30:33], v[14:17], a[8:11]
	ds_read_b128 v[46:49], v167 offset:13312
	v_mfma_f32_16x16x32_f16 a[20:23], v[30:33], v[18:21], a[20:23]
	ds_read_b128 v[50:53], v167 offset:14336
	s_waitcnt lgkmcnt(12)
	v_mfma_f32_16x16x32_f16 a[24:27], v[26:29], v[14:17], a[24:27]
	ds_read_b128 v[62:65], v167 offset:15360
	v_mfma_f32_16x16x32_f16 a[36:39], v[26:29], v[18:21], a[36:39]
	ds_read_b128 v[74:77], v167 offset:16384
	s_waitcnt lgkmcnt(13)
	v_mfma_f32_16x16x32_f16 a[44:47], v[22:25], v[14:17], a[44:47]
	ds_read_b128 v[78:81], v167 offset:17408
	v_mfma_f32_16x16x32_f16 a[64:67], v[22:25], v[18:21], a[64:67]
	s_waitcnt lgkmcnt(13)
	v_mfma_f32_16x16x32_f16 a[32:35], v[10:13], v[14:17], a[32:35]
	v_mfma_f32_16x16x32_f16 a[40:43], v[10:13], v[18:21], a[40:43]
	s_waitcnt lgkmcnt(12)
	v_mfma_f32_16x16x32_f16 a[48:51], v[6:9], v[14:17], a[48:51]
	v_mfma_f32_16x16x32_f16 a[52:55], v[6:9], v[18:21], a[52:55]
	s_waitcnt lgkmcnt(11)
	v_mfma_f32_16x16x32_f16 a[56:59], v[2:5], v[14:17], a[56:59]
	v_mfma_f32_16x16x32_f16 a[68:71], v[2:5], v[18:21], a[68:71]
	s_waitcnt lgkmcnt(8)
	v_mfma_f32_16x16x32_f16 a[0:3], v[70:73], v[82:85], a[0:3]
	ds_read_b128 v[14:17], v150
	v_mfma_f32_16x16x32_f16 a[4:7], v[70:73], v[86:89], a[4:7]
	ds_read_b128 v[18:21], v152
	s_waitcnt lgkmcnt(9)
	v_mfma_f32_16x16x32_f16 a[12:15], v[66:69], v[82:85], a[12:15]
	ds_read_b128 v[42:45], v168
	v_mfma_f32_16x16x32_f16 a[16:19], v[66:69], v[86:89], a[16:19]
	ds_read_b128 v[38:41], v168 offset:1024
	s_waitcnt lgkmcnt(10)
	v_mfma_f32_16x16x32_f16 a[28:31], v[58:61], v[82:85], a[28:31]
	ds_read_b128 v[34:37], v168 offset:2048
	v_mfma_f32_16x16x32_f16 a[60:63], v[58:61], v[86:89], a[60:63]
	ds_read_b128 v[30:33], v168 offset:3072
	s_waitcnt lgkmcnt(11)
	v_mfma_f32_16x16x32_f16 a[8:11], v[54:57], v[82:85], a[8:11]
	ds_read_b128 v[26:29], v168 offset:4096
	v_mfma_f32_16x16x32_f16 a[20:23], v[54:57], v[86:89], a[20:23]
	ds_read_b128 v[22:25], v168 offset:5120
	s_waitcnt lgkmcnt(12)
	v_mfma_f32_16x16x32_f16 a[24:27], v[46:49], v[82:85], a[24:27]
	ds_read_b128 v[10:13], v168 offset:6144
	v_mfma_f32_16x16x32_f16 a[36:39], v[46:49], v[86:89], a[36:39]
	ds_read_b128 v[6:9], v168 offset:7168
	s_waitcnt lgkmcnt(13)
	v_mfma_f32_16x16x32_f16 a[44:47], v[50:53], v[82:85], a[44:47]
	ds_read_b128 v[2:5], v168 offset:8192
	v_mfma_f32_16x16x32_f16 a[64:67], v[50:53], v[86:89], a[64:67]
	s_waitcnt lgkmcnt(13)
	v_mfma_f32_16x16x32_f16 a[32:35], v[62:65], v[82:85], a[32:35]
	v_mfma_f32_16x16x32_f16 a[40:43], v[62:65], v[86:89], a[40:43]
	s_waitcnt lgkmcnt(12)
	v_mfma_f32_16x16x32_f16 a[48:51], v[74:77], v[82:85], a[48:51]
	v_mfma_f32_16x16x32_f16 a[52:55], v[74:77], v[86:89], a[52:55]
	s_waitcnt lgkmcnt(11)
	v_mfma_f32_16x16x32_f16 a[56:59], v[78:81], v[82:85], a[56:59]
	v_mfma_f32_16x16x32_f16 a[68:71], v[78:81], v[86:89], a[68:71]
	s_waitcnt lgkmcnt(8)
	v_mfma_f32_16x16x32_f16 a[0:3], v[42:45], v[14:17], a[0:3]
	ds_read_b128 v[82:85], v151
	v_mfma_f32_16x16x32_f16 a[4:7], v[42:45], v[18:21], a[4:7]
	ds_read_b128 v[86:89], v153
	s_waitcnt lgkmcnt(9)
	v_mfma_f32_16x16x32_f16 a[12:15], v[38:41], v[14:17], a[12:15]
	ds_read_b128 v[70:73], v168 offset:9216
	v_mfma_f32_16x16x32_f16 a[16:19], v[38:41], v[18:21], a[16:19]
	ds_read_b128 v[66:69], v168 offset:10240
	s_waitcnt lgkmcnt(10)
	v_mfma_f32_16x16x32_f16 a[28:31], v[34:37], v[14:17], a[28:31]
	ds_read_b128 v[58:61], v168 offset:11264
	v_mfma_f32_16x16x32_f16 a[60:63], v[34:37], v[18:21], a[60:63]
	ds_read_b128 v[54:57], v168 offset:12288
	s_waitcnt lgkmcnt(11)
	v_mfma_f32_16x16x32_f16 a[8:11], v[30:33], v[14:17], a[8:11]
	ds_read_b128 v[46:49], v168 offset:13312
	v_mfma_f32_16x16x32_f16 a[20:23], v[30:33], v[18:21], a[20:23]
	ds_read_b128 v[50:53], v168 offset:14336
	s_waitcnt lgkmcnt(12)
	v_mfma_f32_16x16x32_f16 a[24:27], v[26:29], v[14:17], a[24:27]
	ds_read_b128 v[62:65], v168 offset:15360
	v_mfma_f32_16x16x32_f16 a[36:39], v[26:29], v[18:21], a[36:39]
	ds_read_b128 v[74:77], v168 offset:16384
	s_waitcnt lgkmcnt(13)
	v_mfma_f32_16x16x32_f16 a[44:47], v[22:25], v[14:17], a[44:47]
	ds_read_b128 v[78:81], v168 offset:17408
	v_mfma_f32_16x16x32_f16 a[64:67], v[22:25], v[18:21], a[64:67]
	s_waitcnt lgkmcnt(13)
	v_mfma_f32_16x16x32_f16 a[32:35], v[10:13], v[14:17], a[32:35]
	v_mfma_f32_16x16x32_f16 a[40:43], v[10:13], v[18:21], a[40:43]
	s_waitcnt lgkmcnt(12)
	v_mfma_f32_16x16x32_f16 a[48:51], v[6:9], v[14:17], a[48:51]
	v_mfma_f32_16x16x32_f16 a[52:55], v[6:9], v[18:21], a[52:55]
	s_waitcnt lgkmcnt(11)
	v_mfma_f32_16x16x32_f16 a[56:59], v[2:5], v[14:17], a[56:59]
	v_mfma_f32_16x16x32_f16 a[68:71], v[2:5], v[18:21], a[68:71]
	s_waitcnt vmcnt(0) lgkmcnt(0)
	s_barrier
	s_add_u32 s52, s50, 0x1f800
	s_addc_u32 s53, s51, 0
	s_add_i32 m0, s42, 0x16000
	s_nop 0
	global_load_lds_dwordx4 v137, s[52:53]
	s_add_i32 m0, s43, 0x16000
	s_nop 0
	global_load_lds_dwordx4 v138, s[52:53]
	s_cmp_lt_u32 s42, 0x800
	s_cbranch_scc0 .Lk4_st4_7
	s_add_i32 m0, s44, 0x16000
	s_nop 0
	global_load_lds_dwordx4 v139, s[52:53]
.Lk4_st4_7:
	v_mfma_f32_16x16x32_f16 a[0:3], v[70:73], v[82:85], a[0:3]
	ds_read_b128 v[14:17], v152
	v_mfma_f32_16x16x32_f16 a[4:7], v[70:73], v[86:89], a[4:7]
	ds_read_b128 v[18:21], v154
	v_mfma_f32_16x16x32_f16 a[12:15], v[66:69], v[82:85], a[12:15]
	ds_read_b128 v[42:45], v164
	v_mfma_f32_16x16x32_f16 a[16:19], v[66:69], v[86:89], a[16:19]
	ds_read_b128 v[38:41], v164 offset:1024
	v_mfma_f32_16x16x32_f16 a[28:31], v[58:61], v[82:85], a[28:31]
	ds_read_b128 v[34:37], v164 offset:2048
	v_mfma_f32_16x16x32_f16 a[60:63], v[58:61], v[86:89], a[60:63]
	ds_read_b128 v[30:33], v164 offset:3072
	v_mfma_f32_16x16x32_f16 a[8:11], v[54:57], v[82:85], a[8:11]
	ds_read_b128 v[26:29], v164 offset:4096
	v_mfma_f32_16x16x32_f16 a[20:23], v[54:57], v[86:89], a[20:23]
	ds_read_b128 v[22:25], v164 offset:5120
	v_mfma_f32_16x16x32_f16 a[24:27], v[46:49], v[82:85], a[24:27]
	ds_read_b128 v[10:13], v164 offset:6144
	v_mfma_f32_16x16x32_f16 a[36:39], v[46:49], v[86:89], a[36:39]
	ds_read_b128 v[6:9], v164 offset:7168
	v_mfma_f32_16x16x32_f16 a[44:47], v[50:53], v[82:85], a[44:47]
	ds_read_b128 v[2:5], v164 offset:8192
	v_mfma_f32_16x16x32_f16 a[64:67], v[50:53], v[86:89], a[64:67]
	v_mfma_f32_16x16x32_f16 a[32:35], v[62:65], v[82:85], a[32:35]
	v_mfma_f32_16x16x32_f16 a[40:43], v[62:65], v[86:89], a[40:43]
	v_mfma_f32_16x16x32_f16 a[48:51], v[74:77], v[82:85], a[48:51]
	v_mfma_f32_16x16x32_f16 a[52:55], v[74:77], v[86:89], a[52:55]
	v_mfma_f32_16x16x32_f16 a[56:59], v[78:81], v[82:85], a[56:59]
	v_mfma_f32_16x16x32_f16 a[68:71], v[78:81], v[86:89], a[68:71]
	s_waitcnt lgkmcnt(8)
	v_mfma_f32_16x16x32_f16 a[0:3], v[42:45], v[14:17], a[0:3]
	ds_read_b128 v[82:85], v153
	v_mfma_f32_16x16x32_f16 a[4:7], v[42:45], v[18:21], a[4:7]
	ds_read_b128 v[86:89], v155
	s_waitcnt lgkmcnt(9)
	v_mfma_f32_16x16x32_f16 a[12:15], v[38:41], v[14:17], a[12:15]
	ds_read_b128 v[70:73], v164 offset:9216
	v_mfma_f32_16x16x32_f16 a[16:19], v[38:41], v[18:21], a[16:19]
	ds_read_b128 v[66:69], v164 offset:10240
	s_waitcnt lgkmcnt(10)
	v_mfma_f32_16x16x32_f16 a[28:31], v[34:37], v[14:17], a[28:31]
	ds_read_b128 v[58:61], v164 offset:11264
	v_mfma_f32_16x16x32_f16 a[60:63], v[34:37], v[18:21], a[60:63]
	ds_read_b128 v[54:57], v164 offset:12288
	s_waitcnt lgkmcnt(11)
	v_mfma_f32_16x16x32_f16 a[8:11], v[30:33], v[14:17], a[8:11]
	ds_read_b128 v[46:49], v164 offset:13312
	v_mfma_f32_16x16x32_f16 a[20:23], v[30:33], v[18:21], a[20:23]
	ds_read_b128 v[50:53], v164 offset:14336
	s_waitcnt lgkmcnt(12)
	v_mfma_f32_16x16x32_f16 a[24:27], v[26:29], v[14:17], a[24:27]
	ds_read_b128 v[62:65], v164 offset:15360
	v_mfma_f32_16x16x32_f16 a[36:39], v[26:29], v[18:21], a[36:39]
	ds_read_b128 v[74:77], v164 offset:16384
	s_waitcnt lgkmcnt(13)
	v_mfma_f32_16x16x32_f16 a[44:47], v[22:25], v[14:17], a[44:47]
	ds_read_b128 v[78:81], v164 offset:17408
	v_mfma_f32_16x16x32_f16 a[64:67], v[22:25], v[18:21], a[64:67]
	s_waitcnt lgkmcnt(13)
	v_mfma_f32_16x16x32_f16 a[32:35], v[10:13], v[14:17], a[32:35]
	v_mfma_f32_16x16x32_f16 a[40:43], v[10:13], v[18:21], a[40:43]
	s_waitcnt lgkmcnt(12)
	v_mfma_f32_16x16x32_f16 a[48:51], v[6:9], v[14:17], a[48:51]
	v_mfma_f32_16x16x32_f16 a[52:55], v[6:9], v[18:21], a[52:55]
	s_waitcnt lgkmcnt(11)
	v_mfma_f32_16x16x32_f16 a[56:59], v[2:5], v[14:17], a[56:59]
	v_mfma_f32_16x16x32_f16 a[68:71], v[2:5], v[18:21], a[68:71]
	s_waitcnt lgkmcnt(8)
	v_mfma_f32_16x16x32_f16 a[0:3], v[70:73], v[82:85], a[0:3]
	ds_read_b128 v[14:17], v156
	v_mfma_f32_16x16x32_f16 a[4:7], v[70:73], v[86:89], a[4:7]
	ds_read_b128 v[18:21], v158
	s_waitcnt lgkmcnt(9)
	v_mfma_f32_16x16x32_f16 a[12:15], v[66:69], v[82:85], a[12:15]
	ds_read_b128 v[42:45], v165
	v_mfma_f32_16x16x32_f16 a[16:19], v[66:69], v[86:89], a[16:19]
	ds_read_b128 v[38:41], v165 offset:1024
	s_waitcnt lgkmcnt(10)
	v_mfma_f32_16x16x32_f16 a[28:31], v[58:61], v[82:85], a[28:31]
	ds_read_b128 v[34:37], v165 offset:2048
	v_mfma_f32_16x16x32_f16 a[60:63], v[58:61], v[86:89], a[60:63]
	ds_read_b128 v[30:33], v165 offset:3072
	s_waitcnt lgkmcnt(11)
	v_mfma_f32_16x16x32_f16 a[8:11], v[54:57], v[82:85], a[8:11]
	ds_read_b128 v[26:29], v165 offset:4096
	v_mfma_f32_16x16x32_f16 a[20:23], v[54:57], v[86:89], a[20:23]
	ds_read_b128 v[22:25], v165 offset:5120
	s_waitcnt lgkmcnt(12)
	v_mfma_f32_16x16x32_f16 a[24:27], v[46:49], v[82:85], a[24:27]
	ds_read_b128 v[10:13], v165 offset:6144
	v_mfma_f32_16x16x32_f16 a[36:39], v[46:49], v[86:89], a[36:39]
	ds_read_b128 v[6:9], v165 offset:7168
	s_waitcnt lgkmcnt(13)
	v_mfma_f32_16x16x32_f16 a[44:47], v[50:53], v[82:85], a[44:47]
	ds_read_b128 v[2:5], v165 offset:8192
	v_mfma_f32_16x16x32_f16 a[64:67], v[50:53], v[86:89], a[64:67]
	s_waitcnt lgkmcnt(13)
	v_mfma_f32_16x16x32_f16 a[32:35], v[62:65], v[82:85], a[32:35]
	v_mfma_f32_16x16x32_f16 a[40:43], v[62:65], v[86:89], a[40:43]
	s_waitcnt lgkmcnt(12)
	v_mfma_f32_16x16x32_f16 a[48:51], v[74:77], v[82:85], a[48:51]
	v_mfma_f32_16x16x32_f16 a[52:55], v[74:77], v[86:89], a[52:55]
	s_waitcnt lgkmcnt(11)
	v_mfma_f32_16x16x32_f16 a[56:59], v[78:81], v[82:85], a[56:59]
	v_mfma_f32_16x16x32_f16 a[68:71], v[78:81], v[86:89], a[68:71]
	s_waitcnt lgkmcnt(8)
	v_mfma_f32_16x16x32_f16 a[0:3], v[42:45], v[14:17], a[0:3]
	ds_read_b128 v[82:85], v157
	v_mfma_f32_16x16x32_f16 a[4:7], v[42:45], v[18:21], a[4:7]
	ds_read_b128 v[86:89], v159
	s_waitcnt lgkmcnt(9)
	v_mfma_f32_16x16x32_f16 a[12:15], v[38:41], v[14:17], a[12:15]
	ds_read_b128 v[70:73], v165 offset:9216
	v_mfma_f32_16x16x32_f16 a[16:19], v[38:41], v[18:21], a[16:19]
	ds_read_b128 v[66:69], v165 offset:10240
	s_waitcnt lgkmcnt(10)
	v_mfma_f32_16x16x32_f16 a[28:31], v[34:37], v[14:17], a[28:31]
	ds_read_b128 v[58:61], v165 offset:11264
	v_mfma_f32_16x16x32_f16 a[60:63], v[34:37], v[18:21], a[60:63]
	ds_read_b128 v[54:57], v165 offset:12288
	s_waitcnt lgkmcnt(11)
	v_mfma_f32_16x16x32_f16 a[8:11], v[30:33], v[14:17], a[8:11]
	ds_read_b128 v[46:49], v165 offset:13312
	v_mfma_f32_16x16x32_f16 a[20:23], v[30:33], v[18:21], a[20:23]
	ds_read_b128 v[50:53], v165 offset:14336
	s_waitcnt lgkmcnt(12)
	v_mfma_f32_16x16x32_f16 a[24:27], v[26:29], v[14:17], a[24:27]
	ds_read_b128 v[62:65], v165 offset:15360
	v_mfma_f32_16x16x32_f16 a[36:39], v[26:29], v[18:21], a[36:39]
	ds_read_b128 v[74:77], v165 offset:16384
	s_waitcnt lgkmcnt(13)
	v_mfma_f32_16x16x32_f16 a[44:47], v[22:25], v[14:17], a[44:47]
	ds_read_b128 v[78:81], v165 offset:17408
	v_mfma_f32_16x16x32_f16 a[64:67], v[22:25], v[18:21], a[64:67]
	s_waitcnt lgkmcnt(13)
	v_mfma_f32_16x16x32_f16 a[32:35], v[10:13], v[14:17], a[32:35]
	v_mfma_f32_16x16x32_f16 a[40:43], v[10:13], v[18:21], a[40:43]
	s_waitcnt lgkmcnt(12)
	v_mfma_f32_16x16x32_f16 a[48:51], v[6:9], v[14:17], a[48:51]
	v_mfma_f32_16x16x32_f16 a[52:55], v[6:9], v[18:21], a[52:55]
	s_waitcnt lgkmcnt(11)
	v_mfma_f32_16x16x32_f16 a[56:59], v[2:5], v[14:17], a[56:59]
	v_mfma_f32_16x16x32_f16 a[68:71], v[2:5], v[18:21], a[68:71]
	s_waitcnt vmcnt(0) lgkmcnt(0)
	s_barrier
	s_add_u32 s52, s50, 0x24000
	s_addc_u32 s53, s51, 0
	s_add_i32 m0, s42, 0xc600
	s_nop 0
	global_load_lds_dwordx4 v137, s[52:53]
	s_add_i32 m0, s43, 0xc600
	s_nop 0
	global_load_lds_dwordx4 v138, s[52:53]
	s_cmp_lt_u32 s42, 0x800
	s_cbranch_scc0 .Lk4_st6_8
	s_add_i32 m0, s44, 0xc600
	s_nop 0
	global_load_lds_dwordx4 v139, s[52:53]
.Lk4_st6_8:
	v_mfma_f32_16x16x32_f16 a[0:3], v[70:73], v[82:85], a[0:3]
	ds_read_b128 v[14:17], v158
	v_mfma_f32_16x16x32_f16 a[4:7], v[70:73], v[86:89], a[4:7]
	ds_read_b128 v[18:21], v160
	v_mfma_f32_16x16x32_f16 a[12:15], v[66:69], v[82:85], a[12:15]
	ds_read_b128 v[42:45], v166
	v_mfma_f32_16x16x32_f16 a[16:19], v[66:69], v[86:89], a[16:19]
	ds_read_b128 v[38:41], v166 offset:1024
	v_mfma_f32_16x16x32_f16 a[28:31], v[58:61], v[82:85], a[28:31]
	ds_read_b128 v[34:37], v166 offset:2048
	v_mfma_f32_16x16x32_f16 a[60:63], v[58:61], v[86:89], a[60:63]
	ds_read_b128 v[30:33], v166 offset:3072
	v_mfma_f32_16x16x32_f16 a[8:11], v[54:57], v[82:85], a[8:11]
	ds_read_b128 v[26:29], v166 offset:4096
	v_mfma_f32_16x16x32_f16 a[20:23], v[54:57], v[86:89], a[20:23]
	ds_read_b128 v[22:25], v166 offset:5120
	v_mfma_f32_16x16x32_f16 a[24:27], v[46:49], v[82:85], a[24:27]
	ds_read_b128 v[10:13], v166 offset:6144
	v_mfma_f32_16x16x32_f16 a[36:39], v[46:49], v[86:89], a[36:39]
	ds_read_b128 v[6:9], v166 offset:7168
	v_mfma_f32_16x16x32_f16 a[44:47], v[50:53], v[82:85], a[44:47]
	ds_read_b128 v[2:5], v166 offset:8192
	v_mfma_f32_16x16x32_f16 a[64:67], v[50:53], v[86:89], a[64:67]
	v_mfma_f32_16x16x32_f16 a[32:35], v[62:65], v[82:85], a[32:35]
	v_mfma_f32_16x16x32_f16 a[40:43], v[62:65], v[86:89], a[40:43]
	v_mfma_f32_16x16x32_f16 a[48:51], v[74:77], v[82:85], a[48:51]
	v_mfma_f32_16x16x32_f16 a[52:55], v[74:77], v[86:89], a[52:55]
	v_mfma_f32_16x16x32_f16 a[56:59], v[78:81], v[82:85], a[56:59]
	v_mfma_f32_16x16x32_f16 a[68:71], v[78:81], v[86:89], a[68:71]
	s_waitcnt lgkmcnt(8)
	v_mfma_f32_16x16x32_f16 a[0:3], v[42:45], v[14:17], a[0:3]
	ds_read_b128 v[82:85], v159
	v_mfma_f32_16x16x32_f16 a[4:7], v[42:45], v[18:21], a[4:7]
	ds_read_b128 v[86:89], v161
	s_waitcnt lgkmcnt(9)
	v_mfma_f32_16x16x32_f16 a[12:15], v[38:41], v[14:17], a[12:15]
	ds_read_b128 v[70:73], v166 offset:9216
	v_mfma_f32_16x16x32_f16 a[16:19], v[38:41], v[18:21], a[16:19]
	ds_read_b128 v[66:69], v166 offset:10240
	s_waitcnt lgkmcnt(10)
	v_mfma_f32_16x16x32_f16 a[28:31], v[34:37], v[14:17], a[28:31]
	ds_read_b128 v[58:61], v166 offset:11264
	v_mfma_f32_16x16x32_f16 a[60:63], v[34:37], v[18:21], a[60:63]
	ds_read_b128 v[54:57], v166 offset:12288
	s_waitcnt lgkmcnt(11)
	v_mfma_f32_16x16x32_f16 a[8:11], v[30:33], v[14:17], a[8:11]
	ds_read_b128 v[46:49], v166 offset:13312
	v_mfma_f32_16x16x32_f16 a[20:23], v[30:33], v[18:21], a[20:23]
	ds_read_b128 v[50:53], v166 offset:14336
	s_waitcnt lgkmcnt(12)
	v_mfma_f32_16x16x32_f16 a[24:27], v[26:29], v[14:17], a[24:27]
	ds_read_b128 v[62:65], v166 offset:15360
	v_mfma_f32_16x16x32_f16 a[36:39], v[26:29], v[18:21], a[36:39]
	ds_read_b128 v[74:77], v166 offset:16384
	s_waitcnt lgkmcnt(13)
	v_mfma_f32_16x16x32_f16 a[44:47], v[22:25], v[14:17], a[44:47]
	ds_read_b128 v[78:81], v166 offset:17408
	v_mfma_f32_16x16x32_f16 a[64:67], v[22:25], v[18:21], a[64:67]
	s_waitcnt lgkmcnt(13)
	v_mfma_f32_16x16x32_f16 a[32:35], v[10:13], v[14:17], a[32:35]
	v_mfma_f32_16x16x32_f16 a[40:43], v[10:13], v[18:21], a[40:43]
	s_waitcnt lgkmcnt(12)
	v_mfma_f32_16x16x32_f16 a[48:51], v[6:9], v[14:17], a[48:51]
	v_mfma_f32_16x16x32_f16 a[52:55], v[6:9], v[18:21], a[52:55]
	s_waitcnt lgkmcnt(11)
	v_mfma_f32_16x16x32_f16 a[56:59], v[2:5], v[14:17], a[56:59]
	v_mfma_f32_16x16x32_f16 a[68:71], v[2:5], v[18:21], a[68:71]
	s_waitcnt vmcnt(0) lgkmcnt(0)
	s_barrier
	v_add_u32_e32 v2, s17, v118
	s_nop 0
	v_readfirstlane_b32 s14, v2
	v_add_u32_e32 v2, s17, v90
	s_mov_b32 m0, s14
	v_readfirstlane_b32 s14, v2
	v_add_u32_e32 v2, s17, v91
	global_load_lds_dwordx4 v[102:103], off nt
	s_mov_b32 m0, s14
	v_readfirstlane_b32 s14, v2
	v_add_u32_e32 v2, s17, v119
	global_load_lds_dwordx4 v[104:105], off nt
	s_mov_b32 m0, s14
	v_readfirstlane_b32 s14, v2
	v_add_u32_e32 v2, s16, v118
	global_load_lds_dwordx4 v[108:109], off nt
	s_mov_b32 m0, s14
	v_readfirstlane_b32 s14, v2
	v_add_u32_e32 v2, s16, v90
	global_load_lds_dwordx4 v[112:113], off nt
	s_mov_b32 m0, s14
	v_readfirstlane_b32 s14, v2
	v_add_u32_e32 v2, s16, v91
	global_load_lds_dwordx4 v[0:1], off nt
	s_mov_b32 m0, s14
	v_readfirstlane_b32 s14, v2
	v_add_u32_e32 v2, s16, v119
	global_load_lds_dwordx4 v[106:107], off nt
	s_mov_b32 m0, s14
	v_readfirstlane_b32 s14, v2
	global_load_lds_dwordx4 v[110:111], off nt
	s_mov_b32 m0, s14
	s_nop 0
	global_load_lds_dwordx4 v[114:115], off nt
	v_mfma_f32_16x16x32_f16 a[0:3], v[70:73], v[82:85], a[0:3]
	ds_read_b128 v[14:17], v160
	v_mfma_f32_16x16x32_f16 a[4:7], v[70:73], v[86:89], a[4:7]
	ds_read_b128 v[18:21], v162
	v_mfma_f32_16x16x32_f16 a[12:15], v[66:69], v[82:85], a[12:15]
	ds_read_b128 v[42:45], v164
	v_mfma_f32_16x16x32_f16 a[16:19], v[66:69], v[86:89], a[16:19]
	ds_read_b128 v[38:41], v164 offset:1024
	v_mfma_f32_16x16x32_f16 a[28:31], v[58:61], v[82:85], a[28:31]
	ds_read_b128 v[34:37], v164 offset:2048
	v_mfma_f32_16x16x32_f16 a[60:63], v[58:61], v[86:89], a[60:63]
	ds_read_b128 v[30:33], v164 offset:3072
	v_mfma_f32_16x16x32_f16 a[8:11], v[54:57], v[82:85], a[8:11]
	ds_read_b128 v[26:29], v164 offset:4096
	v_mfma_f32_16x16x32_f16 a[20:23], v[54:57], v[86:89], a[20:23]
	ds_read_b128 v[22:25], v164 offset:5120
	v_mfma_f32_16x16x32_f16 a[24:27], v[46:49], v[82:85], a[24:27]
	ds_read_b128 v[10:13], v164 offset:6144
	v_mfma_f32_16x16x32_f16 a[36:39], v[46:49], v[86:89], a[36:39]
	ds_read_b128 v[6:9], v164 offset:7168
	v_mfma_f32_16x16x32_f16 a[44:47], v[50:53], v[82:85], a[44:47]
	ds_read_b128 v[2:5], v164 offset:8192
	v_mfma_f32_16x16x32_f16 a[64:67], v[50:53], v[86:89], a[64:67]
	v_mfma_f32_16x16x32_f16 a[32:35], v[62:65], v[82:85], a[32:35]
	v_mfma_f32_16x16x32_f16 a[40:43], v[62:65], v[86:89], a[40:43]
	v_mfma_f32_16x16x32_f16 a[48:51], v[74:77], v[82:85], a[48:51]
	v_mfma_f32_16x16x32_f16 a[52:55], v[74:77], v[86:89], a[52:55]
	v_mfma_f32_16x16x32_f16 a[56:59], v[78:81], v[82:85], a[56:59]
	v_mfma_f32_16x16x32_f16 a[68:71], v[78:81], v[86:89], a[68:71]
	s_waitcnt lgkmcnt(8)
	v_mfma_f32_16x16x32_f16 a[0:3], v[42:45], v[14:17], a[0:3]
	ds_read_b128 v[82:85], v161
	v_mfma_f32_16x16x32_f16 a[4:7], v[42:45], v[18:21], a[4:7]
	ds_read_b128 v[86:89], v163
	s_waitcnt lgkmcnt(9)
	v_mfma_f32_16x16x32_f16 a[12:15], v[38:41], v[14:17], a[12:15]
	ds_read_b128 v[70:73], v164 offset:9216
	v_mfma_f32_16x16x32_f16 a[16:19], v[38:41], v[18:21], a[16:19]
	ds_read_b128 v[66:69], v164 offset:10240
	s_waitcnt lgkmcnt(10)
	v_mfma_f32_16x16x32_f16 a[28:31], v[34:37], v[14:17], a[28:31]
	ds_read_b128 v[58:61], v164 offset:11264
	v_mfma_f32_16x16x32_f16 a[60:63], v[34:37], v[18:21], a[60:63]
	ds_read_b128 v[54:57], v164 offset:12288
	s_waitcnt lgkmcnt(11)
	v_mfma_f32_16x16x32_f16 a[8:11], v[30:33], v[14:17], a[8:11]
	ds_read_b128 v[46:49], v164 offset:13312
	v_mfma_f32_16x16x32_f16 a[20:23], v[30:33], v[18:21], a[20:23]
	ds_read_b128 v[50:53], v164 offset:14336
	s_waitcnt lgkmcnt(12)
	v_mfma_f32_16x16x32_f16 a[24:27], v[26:29], v[14:17], a[24:27]
	ds_read_b128 v[62:65], v164 offset:15360
	v_mfma_f32_16x16x32_f16 a[36:39], v[26:29], v[18:21], a[36:39]
	ds_read_b128 v[74:77], v164 offset:16384
	s_waitcnt lgkmcnt(13)
	v_mfma_f32_16x16x32_f16 a[44:47], v[22:25], v[14:17], a[44:47]
	ds_read_b128 v[78:81], v164 offset:17408
	v_mfma_f32_16x16x32_f16 a[64:67], v[22:25], v[18:21], a[64:67]
	s_waitcnt lgkmcnt(13)
	v_mfma_f32_16x16x32_f16 a[32:35], v[10:13], v[14:17], a[32:35]
	v_mfma_f32_16x16x32_f16 a[40:43], v[10:13], v[18:21], a[40:43]
	s_waitcnt lgkmcnt(12)
	v_mfma_f32_16x16x32_f16 a[48:51], v[6:9], v[14:17], a[48:51]
	v_mfma_f32_16x16x32_f16 a[52:55], v[6:9], v[18:21], a[52:55]
	s_waitcnt lgkmcnt(11)
	v_mfma_f32_16x16x32_f16 a[56:59], v[2:5], v[14:17], a[56:59]
	v_mfma_f32_16x16x32_f16 a[68:71], v[2:5], v[18:21], a[68:71]
	s_waitcnt lgkmcnt(8)
	v_mfma_f32_16x16x32_f16 a[0:3], v[70:73], v[82:85], a[0:3]
	v_mfma_f32_16x16x32_f16 a[4:7], v[70:73], v[86:89], a[4:7]
	s_waitcnt lgkmcnt(9)
	v_mfma_f32_16x16x32_f16 a[12:15], v[66:69], v[82:85], a[12:15]
	v_mfma_f32_16x16x32_f16 a[16:19], v[66:69], v[86:89], a[16:19]
	s_waitcnt lgkmcnt(10)
	v_mfma_f32_16x16x32_f16 a[28:31], v[58:61], v[82:85], a[28:31]
	v_mfma_f32_16x16x32_f16 a[60:63], v[58:61], v[86:89], a[60:63]
	s_waitcnt lgkmcnt(11)
	v_mfma_f32_16x16x32_f16 a[8:11], v[54:57], v[82:85], a[8:11]
	v_mfma_f32_16x16x32_f16 a[20:23], v[54:57], v[86:89], a[20:23]
	s_waitcnt lgkmcnt(12)
	v_mfma_f32_16x16x32_f16 a[24:27], v[46:49], v[82:85], a[24:27]
	v_mfma_f32_16x16x32_f16 a[36:39], v[46:49], v[86:89], a[36:39]
	s_waitcnt lgkmcnt(13)
	v_mfma_f32_16x16x32_f16 a[44:47], v[50:53], v[82:85], a[44:47]
	v_mfma_f32_16x16x32_f16 a[64:67], v[50:53], v[86:89], a[64:67]
	s_waitcnt lgkmcnt(13)
	v_mfma_f32_16x16x32_f16 a[32:35], v[62:65], v[82:85], a[32:35]
	v_mfma_f32_16x16x32_f16 a[40:43], v[62:65], v[86:89], a[40:43]
	s_waitcnt lgkmcnt(12)
	v_mfma_f32_16x16x32_f16 a[48:51], v[74:77], v[82:85], a[48:51]
	v_mfma_f32_16x16x32_f16 a[52:55], v[74:77], v[86:89], a[52:55]
	s_waitcnt lgkmcnt(11)
	v_mfma_f32_16x16x32_f16 a[56:59], v[78:81], v[82:85], a[56:59]
	v_mfma_f32_16x16x32_f16 a[68:71], v[78:81], v[86:89], a[68:71]
	s_waitcnt lgkmcnt(0)
	s_setprio 0

	.amdhsa_kernel _Z7kfinal3PKDF16_PKfS2_S2_PK15HIP_vector_typeIjLj4EES2_Pf
		.amdhsa_group_segment_fixed_size 0
		.amdhsa_private_segment_fixed_size 0
		.amdhsa_kernarg_size 56
		.amdhsa_user_sgpr_count 2
		.amdhsa_user_sgpr_dispatch_ptr 0
		.amdhsa_user_sgpr_queue_ptr 0
		.amdhsa_user_sgpr_kernarg_segment_ptr 1
		.amdhsa_user_sgpr_dispatch_id 0
		.amdhsa_user_sgpr_kernarg_preload_length 0
		.amdhsa_user_sgpr_kernarg_preload_offset 0
		.amdhsa_user_sgpr_private_segment_size 0
		.amdhsa_uses_dynamic_stack 0
		.amdhsa_enable_private_segment 0
		.amdhsa_system_sgpr_workgroup_id_x 1
		.amdhsa_system_sgpr_workgroup_id_y 0
		.amdhsa_system_sgpr_workgroup_id_z 0
		.amdhsa_system_sgpr_workgroup_info 0
		.amdhsa_system_vgpr_workitem_id 0
		.amdhsa_next_free_vgpr 245
		.amdhsa_next_free_sgpr 54
		.amdhsa_accum_offset 172
		.amdhsa_reserve_vcc 1
		.amdhsa_float_round_mode_32 0
		.amdhsa_float_round_mode_16_64 0
		.amdhsa_float_denorm_mode_32 3
		.amdhsa_float_denorm_mode_16_64 3
		.amdhsa_dx10_clamp 1
		.amdhsa_ieee_mode 1
		.amdhsa_fp16_overflow 0
		.amdhsa_tg_split 0
		.amdhsa_exception_fp_ieee_invalid_op 0
		.amdhsa_exception_fp_denorm_src 0
		.amdhsa_exception_fp_ieee_div_zero 0
		.amdhsa_exception_fp_ieee_overflow 0
		.amdhsa_exception_fp_ieee_underflow 0
		.amdhsa_exception_fp_ieee_inexact 0
		.amdhsa_exception_int_div_zero 0
	.end_amdhsa_kernel

amdhsa.kernels:
  - .agpr_count:     0
    .args:
      - .actual_access:  read_only
        .address_space:  global
        .offset:         0
        .size:           8
        .value_kind:     global_buffer
      - .actual_access:  read_only
        .address_space:  global
        .offset:         8
        .size:           8
        .value_kind:     global_buffer
      - .actual_access:  read_only
        .address_space:  global
        .offset:         16
        .size:           8
        .value_kind:     global_buffer
      - .actual_access:  read_only
        .address_space:  global
        .offset:         24
        .size:           8
        .value_kind:     global_buffer
      - .actual_access:  read_only
        .address_space:  global
        .offset:         32
        .size:           8
        .value_kind:     global_buffer
      - .actual_access:  read_only
        .address_space:  global
        .offset:         40
        .size:           8
        .value_kind:     global_buffer
      - .actual_access:  write_only
        .address_space:  global
        .offset:         48
        .size:           8
        .value_kind:     global_buffer
      - .actual_access:  write_only
        .address_space:  global
        .offset:         56
        .size:           8
        .value_kind:     global_buffer
      - .actual_access:  write_only
        .address_space:  global
        .offset:         64
        .size:           8
        .value_kind:     global_buffer
      - .actual_access:  write_only
        .address_space:  global
        .offset:         72
        .size:           8
        .value_kind:     global_buffer
    .group_segment_fixed_size: 12000
    .kernarg_segment_align: 8
    .kernarg_segment_size: 80
    .language:       OpenCL C
    .language_version:
      - 2
      - 0
    .max_flat_workgroup_size: 256
    .name:           _Z2k0PKfS0_S0_S0_S0_S0_PDF16_PfS1_S1_
    .private_segment_fixed_size: 0
    .sgpr_count:     24
    .sgpr_spill_count: 0
    .symbol:         _Z2k0PKfS0_S0_S0_S0_S0_PDF16_PfS1_S1_.kd
    .uniform_work_group_size: 1
    .uses_dynamic_stack: false
    .vgpr_count:     150
    .vgpr_spill_count: 0
    .wavefront_size: 64
  - .agpr_count:     16
    .args:
      - .actual_access:  read_only
        .address_space:  global
        .offset:         0
        .size:           8
        .value_kind:     global_buffer
      - .actual_access:  read_only
        .address_space:  global
        .offset:         8
        .size:           8
        .value_kind:     global_buffer
      - .actual_access:  read_only
        .address_space:  global
        .offset:         16
        .size:           8
        .value_kind:     global_buffer
      - .actual_access:  read_only
        .address_space:  global
        .offset:         24
        .size:           8
        .value_kind:     global_buffer
      - .actual_access:  read_only
        .address_space:  global
        .offset:         32
        .size:           8
        .value_kind:     global_buffer
      - .actual_access:  write_only
        .address_space:  global
        .offset:         40
        .size:           8
        .value_kind:     global_buffer
      - .actual_access:  write_only
        .address_space:  global
        .offset:         48
        .size:           8
        .value_kind:     global_buffer
    .group_segment_fixed_size: 14112
    .kernarg_segment_align: 8
    .kernarg_segment_size: 56
    .language:       OpenCL C
    .language_version:
      - 2
      - 0
    .max_flat_workgroup_size: 256
    .name:           _Z4khidPKDF16_PKfS2_S2_S0_PDF16_Pf
    .private_segment_fixed_size: 0
    .sgpr_count:     24
    .sgpr_spill_count: 0
    .symbol:         _Z4khidPKDF16_PKfS2_S2_S0_PDF16_Pf.kd
    .uniform_work_group_size: 1
    .uses_dynamic_stack: false
    .vgpr_count:     148
    .vgpr_spill_count: 0
    .wavefront_size: 64
  - .agpr_count:     144
    .args:
      - .actual_access:  read_only
        .address_space:  global
        .offset:         0
        .size:           8
        .value_kind:     global_buffer
      - .actual_access:  read_only
        .address_space:  global
        .offset:         8
        .size:           8
        .value_kind:     global_buffer
      - .actual_access:  read_only
        .address_space:  global
        .offset:         16
        .size:           8
        .value_kind:     global_buffer
      - .actual_access:  read_only
        .address_space:  global
        .offset:         24
        .size:           8
        .value_kind:     global_buffer
      - .address_space:  global
        .offset:         32
        .size:           8
        .value_kind:     global_buffer
      - .address_space:  global
        .offset:         40
        .size:           8
        .value_kind:     global_buffer
      - .address_space:  global
        .offset:         48
        .size:           8
        .value_kind:     global_buffer
    .group_segment_fixed_size: 0
    .kernarg_segment_align: 8
    .kernarg_segment_size: 56
    .language:       OpenCL C
    .language_version:
      - 2
      - 0
    .max_flat_workgroup_size: 256
    .name:           _Z6kfinalPKDF16_PKfS2_S2_PK15HIP_vector_typeIjLj4EES2_Pf
    .private_segment_fixed_size: 0
    .sgpr_count:     41
    .sgpr_spill_count: 0
    .symbol:         _Z6kfinalPKDF16_PKfS2_S2_PK15HIP_vector_typeIjLj4EES2_Pf.kd
    .uniform_work_group_size: 1
    .uses_dynamic_stack: false
    .vgpr_count:     400
    .vgpr_spill_count: 0
    .wavefront_size: 64
  - .agpr_count:     73
    .args:
      - .actual_access:  read_only
        .address_space:  global
        .offset:         0
        .size:           8
        .value_kind:     global_buffer
      - .actual_access:  read_only
        .address_space:  global
        .offset:         8
        .size:           8
        .value_kind:     global_buffer
      - .actual_access:  read_only
        .address_space:  global
        .offset:         16
        .size:           8
        .value_kind:     global_buffer
      - .actual_access:  read_only
        .address_space:  global
        .offset:         24
        .size:           8
        .value_kind:     global_buffer
      - .address_space:  global
        .offset:         32
        .size:           8
        .value_kind:     global_buffer
      - .address_space:  global
        .offset:         40
        .size:           8
        .value_kind:     global_buffer
      - .address_space:  global
        .offset:         48
        .size:           8
        .value_kind:     global_buffer
    .group_segment_fixed_size: 0
    .kernarg_segment_align: 8
    .kernarg_segment_size: 56
    .language:       OpenCL C
    .language_version:
      - 2
      - 0
    .max_flat_workgroup_size: 512
    .name:           _Z7kfinal3PKDF16_PKfS2_S2_PK15HIP_vector_typeIjLj4EES2_Pf
    .private_segment_fixed_size: 0
    .sgpr_count:     60
    .sgpr_spill_count: 0
    .symbol:         _Z7kfinal3PKDF16_PKfS2_S2_PK15HIP_vector_typeIjLj4EES2_Pf.kd
    .uniform_work_group_size: 1
    .uses_dynamic_stack: false
    .vgpr_count:     245
    .vgpr_spill_count: 0
    .wavefront_size: 64
